# code placement: step head +8 bytes, flush head +12 bytes (all hot loop heads at 4 mod 8)
# baseline (speedup 1.0000x reference)
.LBB1_143:
	s_or_b64 exec, exec, s[2:3]
	v_cndmask_b32_e64 v24, v14, 0, s[4:5]
	v_ashrrev_i32_e32 v25, 31, v24
	v_lshlrev_b64 v[24:25], 3, v[24:25]
	s_mov_b64 s[2:3], src_shared_base
	v_lshl_add_u64 v[24:25], s[56:57], 0, v[24:25]
	v_mov_b32_e32 v14, s3
	v_cndmask_b32_e64 v232, v24, 0, s[4:5]
	v_add_lshl_u32 v24, s13, v1, 1
	v_cndmask_b32_e64 v233, v25, v14, s[4:5]
	s_mov_b32 s81, s4
	s_nop 0
	s_nop 0
	v_ashrrev_i32_e32 v25, 31, v24
	v_lshl_add_u64 v[24:25], v[24:25], 2, v[232:233]
	flat_load_dwordx2 v[82:83], v[24:25]
	s_mov_b32 s2, 0x4038aa3b
	v_add_f32_e32 v239, s33, v11
	s_waitcnt vmcnt(0)
	v_fma_mixlo_f16 v11, v18, s2, 0
	v_fma_mixlo_f16 v25, v16, s2, 0
	v_fma_mixlo_f16 v27, v17, s2, 0
	v_add_lshl_u32 v22, s13, v22, 1
	v_fma_mixlo_f16 v14, v19, s2, 0
	v_fma_mixlo_f16 v18, v18, s2, -v11 op_sel_hi:[0,0,1]
	v_fma_mixlo_f16 v16, v16, s2, -v25 op_sel_hi:[0,0,1]
	v_fma_mixlo_f16 v17, v17, s2, -v27 op_sel_hi:[0,0,1]
	s_mov_b32 s14, 0x186a0
	v_ashrrev_i32_e32 v23, 31, v22
	v_fma_mixlo_f16 v19, v19, s2, -v14 op_sel_hi:[0,0,1]
	v_cndmask_b32_e64 v11, 0, v11, s[0:1]
	v_cndmask_b32_e64 v14, 0, v14, s[0:1]
	v_cndmask_b32_e64 v25, 0, v25, s[0:1]
	v_cndmask_b32_e64 v27, 0, v27, s[0:1]
	v_cndmask_b32_e64 v18, 0, v18, s[0:1]
	v_cndmask_b32_e64 v16, 0, v16, s[0:1]
	v_cndmask_b32_e64 v17, 0, v17, s[0:1]
	v_pack_b32_f16 v179, v11, v14
	v_pack_b32_f16 v178, v11, v18
	v_pack_b32_f16 v185, v27, v17
	v_pack_b32_f16 v182, v25, v16
	v_lshl_add_u64 v[16:17], v[22:23], 2, v[232:233]
	flat_load_dwordx2 v[236:237], v[16:17]
	v_mov_b32_e32 v17, v2
	v_cndmask_b32_e64 v19, 0, v19, s[0:1]
	v_pack_b32_f16 v180, v19, v14
	v_fma_mixlo_f16 v14, v13, s2, 0
	v_fma_mixlo_f16 v13, v13, s2, -v14 op_sel_hi:[0,0,1]
	v_cndmask_b32_e64 v14, 0, v14, s[0:1]
	v_cndmask_b32_e64 v13, 0, v13, s[0:1]
	v_fma_mixlo_f16 v24, v20, s2, 0
	v_fma_mixlo_f16 v26, v21, s2, 0
	v_or_b32_e32 v240, 64, v1
	v_pack_b32_f16 v188, v13, v14
	v_fma_mixlo_f16 v13, v10, s2, 0
	v_lshl_add_u32 v244, v1, 2, v3
	v_and_b32_e32 v0, 32, v0
	v_mov_b32_e32 v1, 0xa300
	v_fma_mixlo_f16 v20, v20, s2, -v24 op_sel_hi:[0,0,1]
	v_fma_mixlo_f16 v21, v21, s2, -v26 op_sel_hi:[0,0,1]
	v_fma_mixlo_f16 v10, v10, s2, -v13 op_sel_hi:[0,0,1]
	v_lshl_or_b32 v245, v0, 2, v1
	v_lshl_add_u32 v246, v8, 4, v1
	v_add_u32_e32 v3, 64, v7
	v_cndmask_b32_e64 v24, 0, v24, s[0:1]
	v_cndmask_b32_e64 v26, 0, v26, s[0:1]
	v_cndmask_b32_e64 v20, 0, v20, s[0:1]
	v_cndmask_b32_e64 v21, 0, v21, s[0:1]
	v_cndmask_b32_e64 v13, 0, v13, s[0:1]
	v_cndmask_b32_e64 v10, 0, v10, s[0:1]
	v_mov_b32_e32 v0, 0xc0
	v_pack_b32_f16 v183, v25, v26
	v_pack_b32_f16 v181, v24, v20
	v_pack_b32_f16 v184, v21, v26
	v_pack_b32_f16 v193, v13, v10
	v_lshlrev_b32_e32 v251, 3, v9
	v_mov_b32_e32 v7, v2
	v_mov_b32_e32 v9, v2
	v_mov_b32_e32 v10, v2
	v_mov_b32_e32 v13, v2
	v_add_u32_e32 v242, 8, v251
	s_waitcnt lgkmcnt(0)
	v_sub_u32_e32 v234, v231, v230
	s_mov_b64 s[4:5], 0
	v_mov_b32_e32 v249, s6
	s_mov_b32 s71, s6
	v_mov_b32_e32 v231, s13
	s_mov_b32 s70, s13
	s_mov_b32 s15, 0x5040100
	s_mov_b32 s82, 1.0
	s_mov_b32 s83, 1.0
	s_mov_b32 s73, 0x3c000000
	s_mov_b32 s74, 0x42004000
	s_mov_b32 s75, 0x48804800
	s_mov_b32 s76, 0x49804900
	s_mov_b32 s77, 0x4c404c00
	s_mov_b32 s78, 0x4cc04c80
	s_mov_b32 s79, 0x4e404e00
	s_mov_b32 s80, 0x4ec04e80
	v_mov_b32_e32 v197, 0x3c003c00
	s_mov_b32 s16, 0x10000
	s_mov_b32 s17, 0x7a100
	v_lshl_or_b32 v11, v82, 3, 3
	v_cmp_gt_u32_e32 vcc, s14, v82
	v_mov_b32_e32 v196, v83
	s_nop 0
	v_cndmask_b32_e32 v16, 3, v11, vcc
	v_lshl_add_u64 v[16:17], v[16:17], 2, s[54:55]
	global_load_dword v241, v[16:17], off
	v_fma_mixlo_f16 v11, v12, s2, 0
	v_fma_mixlo_f16 v12, v12, s2, -v11 op_sel_hi:[0,0,1]
	v_cndmask_b32_e64 v11, 0, v11, s[0:1]
	v_cndmask_b32_e64 v12, 0, v12, s[0:1]
	v_pack_b32_f16 v187, v11, v14
	v_pack_b32_f16 v186, v11, v12
	v_fma_mixlo_f16 v11, v4, s2, 0
	v_fma_mixlo_f16 v4, v4, s2, -v11 op_sel_hi:[0,0,1]
	v_cndmask_b32_e64 v11, 0, v11, s[0:1]
	v_cndmask_b32_e64 v4, 0, v4, s[0:1]
	v_fma_mixlo_f16 v16, v15, s2, 0
	v_pack_b32_f16 v190, v11, v4
	v_lshrrev_b32_e32 v4, 3, v8
	v_fma_mixlo_f16 v15, v15, s2, -v16 op_sel_hi:[0,0,1]
	v_fma_mixlo_f16 v12, v5, s2, 0
	v_and_b32_e32 v243, 4, v4
	v_cndmask_b32_e64 v16, 0, v16, s[0:1]
	v_cndmask_b32_e64 v15, 0, v15, s[0:1]
	v_fma_mixlo_f16 v5, v5, s2, -v12 op_sel_hi:[0,0,1]
	v_lshl_add_u32 v247, v243, 6, v1
	v_xor_b32_e32 v1, 32, v6
	v_pack_b32_f16 v189, v16, v15
	v_cndmask_b32_e64 v12, 0, v12, s[0:1]
	v_cndmask_b32_e64 v5, 0, v5, s[0:1]
	v_cmp_lt_i32_e32 vcc, v1, v3
	v_mov_b32_e32 v16, v2
	v_mov_b32_e32 v17, v2
	v_pack_b32_f16 v191, v11, v12
	v_pack_b32_f16 v192, v5, v12
	v_lshl_or_b32 v0, v4, 6, v0
	v_cndmask_b32_e32 v1, v6, v1, vcc
	v_mov_b32_e32 v3, v2
	v_mov_b32_e32 v4, v2
	v_mov_b32_e32 v5, v2
	v_mov_b32_e32 v6, v2
	v_mov_b32_e32 v8, v2
	v_mov_b32_e32 v11, v2
	v_mov_b32_e32 v12, v2
	v_mov_b32_e32 v14, v2
	v_mov_b32_e32 v15, v2
	v_mov_b64_e32 v[32:33], v[16:17]
	v_mov_b64_e32 v[48:49], v[16:17]
	v_mov_b64_e32 v[64:65], v[16:17]
	v_mov_b64_e32 v[80:81], v[16:17]
	v_lshlrev_b32_e32 v248, 2, v1
	v_add_u32_e32 v250, 0xa300, v0
	v_mov_b64_e32 v[30:31], v[14:15]
	v_mov_b64_e32 v[28:29], v[12:13]
	v_mov_b64_e32 v[26:27], v[10:11]
	v_mov_b64_e32 v[24:25], v[8:9]
	v_mov_b64_e32 v[22:23], v[6:7]
	v_mov_b64_e32 v[20:21], v[4:5]
	v_mov_b64_e32 v[18:19], v[2:3]
	v_mov_b64_e32 v[46:47], v[14:15]
	v_mov_b64_e32 v[44:45], v[12:13]
	v_mov_b64_e32 v[42:43], v[10:11]
	v_mov_b64_e32 v[40:41], v[8:9]
	v_mov_b64_e32 v[38:39], v[6:7]
	v_mov_b64_e32 v[36:37], v[4:5]
	v_mov_b64_e32 v[34:35], v[2:3]
	v_mov_b64_e32 v[62:63], v[14:15]
	v_mov_b64_e32 v[60:61], v[12:13]
	v_mov_b64_e32 v[58:59], v[10:11]
	v_mov_b64_e32 v[56:57], v[8:9]
	v_mov_b64_e32 v[54:55], v[6:7]
	v_mov_b64_e32 v[52:53], v[4:5]
	v_mov_b64_e32 v[50:51], v[2:3]
	v_mov_b64_e32 v[78:79], v[14:15]
	v_mov_b64_e32 v[76:77], v[12:13]
	v_mov_b64_e32 v[74:75], v[10:11]
	v_mov_b64_e32 v[72:73], v[8:9]
	v_mov_b64_e32 v[70:71], v[6:7]
	v_mov_b64_e32 v[68:69], v[4:5]
	v_mov_b64_e32 v[66:67], v[2:3]
	s_branch .LBB1_145
